# MoE K-loops: per staged weight load wait->convert->ds_write->re-issue interleaved into MFMA block 4, tail address arithmetic moved to the segment start
# speedup vs baseline: 1.0263x; 1.0131x over previous
.LBB0_726:
	s_cmp_lg_u64 s[2:3], 0
	s_cbranch_scc1 .Lswp_guE_half
	ds_read_b64_tr_b16 v[162:163], v190 offset:0
	ds_read_b64_tr_b16 v[164:165], v191 offset:0
	ds_read_b64_tr_b16 v[166:167], v190 offset:8192
	ds_read_b64_tr_b16 v[168:169], v191 offset:8192
	ds_read_b64_tr_b16 v[170:171], v192 offset:0
	ds_read_b64_tr_b16 v[172:173], v193 offset:0
	ds_read_b64_tr_b16 v[174:175], v192 offset:8192
	ds_read_b64_tr_b16 v[176:177], v193 offset:8192
	ds_read_b128 v[214:217], v207
	ds_read_b128 v[224:227], v207 offset:2048
	ds_read_b128 v[232:235], v207 offset:4096
	ds_read_b128 v[240:243], v207 offset:6144
	ds_read_b128 v[218:221], v207 offset:1024
	ds_read_b128 v[228:231], v207 offset:3072
	ds_read_b128 v[236:239], v207 offset:5120
	ds_read_b128 v[244:247], v207 offset:7168
	s_add_i32 s38, s4, 2
	s_cmp_eq_u32 s34, 28
	s_cselect_b64 s[4:5], -1, 0
	s_and_b64 s[34:35], s[4:5], exec
	s_cselect_b32 s38, 0, s38
	s_cselect_b32 s34, s23, s37
	s_cselect_b32 s35, s22, s36
	s_cselect_b32 s66, s21, s25
	s_cselect_b32 s67, s20, s24
	s_ashr_i32 s39, s38, 31
	s_lshl_b64 s[40:41], s[38:39], 18
	s_add_u32 s68, s67, s40
	s_addc_u32 s69, s66, s41
	s_add_u32 s40, s35, s40
	s_addc_u32 s41, s34, s41
	s_setprio 1
	s_waitcnt lgkmcnt(7)
	v_mfma_f32_16x16x32_bf16 v[158:161], v[162:165], v[214:217], v[158:161]
	v_mfma_f32_16x16x32_bf16 v[154:157], v[170:173], v[214:217], v[154:157]
	ds_read_b128 v[214:217], v207 offset:16384
	s_waitcnt lgkmcnt(7)
	v_mfma_f32_16x16x32_bf16 v[146:149], v[162:165], v[224:227], v[146:149]
	v_mfma_f32_16x16x32_bf16 v[138:141], v[170:173], v[224:227], v[138:141]
	ds_read_b128 v[224:227], v207 offset:18432
	s_waitcnt lgkmcnt(7)
	v_mfma_f32_16x16x32_bf16 v[130:133], v[162:165], v[232:235], v[130:133]
	v_mfma_f32_16x16x32_bf16 v[122:125], v[170:173], v[232:235], v[122:125]
	ds_read_b128 v[232:235], v207 offset:20480
	s_waitcnt lgkmcnt(7)
	v_mfma_f32_16x16x32_bf16 v[114:117], v[162:165], v[240:243], v[114:117]
	v_mfma_f32_16x16x32_bf16 v[106:109], v[170:173], v[240:243], v[106:109]
	ds_read_b128 v[240:243], v207 offset:22528
	s_waitcnt lgkmcnt(7)
	v_mfma_f32_16x16x32_bf16 v[158:161], v[166:169], v[218:221], v[158:161]
	v_mfma_f32_16x16x32_bf16 v[154:157], v[174:177], v[218:221], v[154:157]
	ds_read_b128 v[218:221], v207 offset:17408
	s_waitcnt lgkmcnt(7)
	v_mfma_f32_16x16x32_bf16 v[146:149], v[166:169], v[228:231], v[146:149]
	v_mfma_f32_16x16x32_bf16 v[138:141], v[174:177], v[228:231], v[138:141]
	ds_read_b128 v[228:231], v207 offset:19456
	s_waitcnt lgkmcnt(7)
	v_mfma_f32_16x16x32_bf16 v[130:133], v[166:169], v[236:239], v[130:133]
	v_mfma_f32_16x16x32_bf16 v[122:125], v[174:177], v[236:239], v[122:125]
	ds_read_b128 v[236:239], v207 offset:21504
	s_waitcnt lgkmcnt(7)
	v_mfma_f32_16x16x32_bf16 v[114:117], v[166:169], v[244:247], v[114:117]
	v_mfma_f32_16x16x32_bf16 v[106:109], v[174:177], v[244:247], v[106:109]
	ds_read_b128 v[244:247], v207 offset:23552
	s_waitcnt lgkmcnt(7)
	v_mfma_f32_16x16x32_bf16 v[94:97], v[162:165], v[214:217], v[94:97]
	v_mfma_f32_16x16x32_bf16 v[86:89], v[170:173], v[214:217], v[86:89]
	ds_read_b128 v[214:217], v207
	s_waitcnt lgkmcnt(7)
	v_mfma_f32_16x16x32_bf16 v[78:81], v[162:165], v[224:227], v[78:81]
	v_mfma_f32_16x16x32_bf16 v[70:73], v[170:173], v[224:227], v[70:73]
	ds_read_b128 v[224:227], v207 offset:2048
	s_waitcnt lgkmcnt(7)
	v_mfma_f32_16x16x32_bf16 v[62:65], v[162:165], v[232:235], v[62:65]
	v_mfma_f32_16x16x32_bf16 v[54:57], v[170:173], v[232:235], v[54:57]
	ds_read_b128 v[232:235], v207 offset:4096
	s_waitcnt lgkmcnt(7)
	v_mfma_f32_16x16x32_bf16 v[46:49], v[162:165], v[240:243], v[46:49]
	v_mfma_f32_16x16x32_bf16 v[38:41], v[170:173], v[240:243], v[38:41]
	ds_read_b128 v[240:243], v207 offset:6144
	ds_read_b64_tr_b16 v[162:163], v190 offset:16384
	ds_read_b64_tr_b16 v[164:165], v191 offset:16384
	ds_read_b64_tr_b16 v[170:171], v192 offset:16384
	ds_read_b64_tr_b16 v[172:173], v193 offset:16384
	s_waitcnt lgkmcnt(11)
	v_mfma_f32_16x16x32_bf16 v[94:97], v[166:169], v[218:221], v[94:97]
	v_mfma_f32_16x16x32_bf16 v[86:89], v[174:177], v[218:221], v[86:89]
	ds_read_b128 v[218:221], v207 offset:1024
	s_waitcnt lgkmcnt(11)
	v_mfma_f32_16x16x32_bf16 v[78:81], v[166:169], v[228:231], v[78:81]
	v_mfma_f32_16x16x32_bf16 v[70:73], v[174:177], v[228:231], v[70:73]
	ds_read_b128 v[228:231], v207 offset:3072
	s_waitcnt lgkmcnt(11)
	v_mfma_f32_16x16x32_bf16 v[62:65], v[166:169], v[236:239], v[62:65]
	v_mfma_f32_16x16x32_bf16 v[54:57], v[174:177], v[236:239], v[54:57]
	ds_read_b128 v[236:239], v207 offset:5120
	s_waitcnt lgkmcnt(11)
	v_mfma_f32_16x16x32_bf16 v[46:49], v[166:169], v[244:247], v[46:49]
	v_mfma_f32_16x16x32_bf16 v[38:41], v[174:177], v[244:247], v[38:41]
	ds_read_b128 v[244:247], v207 offset:7168
	ds_read_b64_tr_b16 v[166:167], v190 offset:24576
	ds_read_b64_tr_b16 v[168:169], v191 offset:24576
	ds_read_b64_tr_b16 v[174:175], v192 offset:24576
	ds_read_b64_tr_b16 v[176:177], v193 offset:24576
	s_waitcnt lgkmcnt(8)
	v_mfma_f32_16x16x32_bf16 v[150:153], v[162:165], v[214:217], v[150:153]
	v_mfma_f32_16x16x32_bf16 v[142:145], v[170:173], v[214:217], v[142:145]
	ds_read_b128 v[214:217], v207 offset:16384
	v_mfma_f32_16x16x32_bf16 v[134:137], v[162:165], v[224:227], v[134:137]
	v_mfma_f32_16x16x32_bf16 v[126:129], v[170:173], v[224:227], v[126:129]
	ds_read_b128 v[224:227], v207 offset:18432
	v_mfma_f32_16x16x32_bf16 v[118:121], v[162:165], v[232:235], v[118:121]
	v_mfma_f32_16x16x32_bf16 v[110:113], v[170:173], v[232:235], v[110:113]
	ds_read_b128 v[232:235], v207 offset:20480
	v_mfma_f32_16x16x32_bf16 v[102:105], v[162:165], v[240:243], v[102:105]
	v_mfma_f32_16x16x32_bf16 v[98:101], v[170:173], v[240:243], v[98:101]
	ds_read_b128 v[240:243], v207 offset:22528
	s_waitcnt lgkmcnt(4)
	v_mfma_f32_16x16x32_bf16 v[150:153], v[166:169], v[218:221], v[150:153]
	v_mfma_f32_16x16x32_bf16 v[142:145], v[174:177], v[218:221], v[142:145]
	ds_read_b128 v[218:221], v207 offset:17408
	v_mfma_f32_16x16x32_bf16 v[134:137], v[166:169], v[228:231], v[134:137]
	v_mfma_f32_16x16x32_bf16 v[126:129], v[174:177], v[228:231], v[126:129]
	ds_read_b128 v[228:231], v207 offset:19456
	v_mfma_f32_16x16x32_bf16 v[118:121], v[166:169], v[236:239], v[118:121]
	v_mfma_f32_16x16x32_bf16 v[110:113], v[174:177], v[236:239], v[110:113]
	ds_read_b128 v[236:239], v207 offset:21504
	v_mfma_f32_16x16x32_bf16 v[102:105], v[166:169], v[244:247], v[102:105]
	v_mfma_f32_16x16x32_bf16 v[98:101], v[174:177], v[244:247], v[98:101]
	ds_read_b128 v[244:247], v207 offset:23552
	s_waitcnt lgkmcnt(7)
	v_mfma_f32_16x16x32_bf16 v[90:93], v[162:165], v[214:217], v[90:93]
	v_mfma_f32_16x16x32_bf16 v[82:85], v[170:173], v[214:217], v[82:85]
	s_waitcnt vmcnt(11)
	v_cvt_pk_bf16_f32 v248, v2, v3
	v_cvt_pk_bf16_f32 v249, v4, v5
	ds_write_b64 v199, v[248:249]
	s_add_u32 s70, s40, 0x6000
	s_addc_u32 s71, s41, 0
	global_load_dwordx4 v[2:5], v189, s[70:71]
	s_waitcnt lgkmcnt(7)
	v_mfma_f32_16x16x32_bf16 v[74:77], v[162:165], v[224:227], v[74:77]
	v_mfma_f32_16x16x32_bf16 v[66:69], v[170:173], v[224:227], v[66:69]
	s_waitcnt vmcnt(11)
	v_cvt_pk_bf16_f32 v248, v6, v7
	v_cvt_pk_bf16_f32 v249, v8, v9
	ds_write_b64 v200, v[248:249]
	s_add_u32 s72, s40, 0x4000
	s_addc_u32 s73, s41, 0
	global_load_dwordx4 v[6:9], v189, s[72:73]
	s_waitcnt lgkmcnt(7)
	v_mfma_f32_16x16x32_bf16 v[58:61], v[162:165], v[232:235], v[58:61]
	v_mfma_f32_16x16x32_bf16 v[50:53], v[170:173], v[232:235], v[50:53]
	s_waitcnt vmcnt(11)
	v_cvt_pk_bf16_f32 v248, v10, v11
	v_cvt_pk_bf16_f32 v249, v12, v13
	ds_write_b64 v201, v[248:249]
	s_add_u32 s70, s68, 0x6000
	s_addc_u32 s71, s69, 0
	global_load_dwordx4 v[10:13], v189, s[70:71]
	s_waitcnt lgkmcnt(7)
	v_mfma_f32_16x16x32_bf16 v[42:45], v[162:165], v[240:243], v[42:45]
	v_mfma_f32_16x16x32_bf16 v[30:33], v[170:173], v[240:243], v[30:33]
	s_waitcnt vmcnt(11)
	v_cvt_pk_bf16_f32 v248, v14, v15
	v_cvt_pk_bf16_f32 v249, v16, v17
	ds_write_b64 v202, v[248:249]
	s_add_u32 s72, s40, 0x2000
	s_addc_u32 s73, s41, 0
	global_load_dwordx4 v[14:17], v189, s[72:73]
	s_waitcnt lgkmcnt(7)
	v_mfma_f32_16x16x32_bf16 v[90:93], v[166:169], v[218:221], v[90:93]
	v_mfma_f32_16x16x32_bf16 v[82:85], v[174:177], v[218:221], v[82:85]
	s_waitcnt vmcnt(11)
	v_cvt_pk_bf16_f32 v248, v18, v19
	v_cvt_pk_bf16_f32 v249, v20, v21
	ds_write_b64 v203, v[248:249]
	s_add_u32 s70, s68, 0x4000
	s_addc_u32 s71, s69, 0
	global_load_dwordx4 v[18:21], v189, s[70:71]
	s_waitcnt lgkmcnt(7)
	v_mfma_f32_16x16x32_bf16 v[74:77], v[166:169], v[228:231], v[74:77]
	v_mfma_f32_16x16x32_bf16 v[66:69], v[174:177], v[228:231], v[66:69]
	s_waitcnt vmcnt(11)
	v_cvt_pk_bf16_f32 v248, v22, v23
	v_cvt_pk_bf16_f32 v249, v24, v25
	ds_write_b64 v204, v[248:249]
	global_load_dwordx4 v[22:25], v189, s[40:41]
	s_waitcnt lgkmcnt(7)
	v_mfma_f32_16x16x32_bf16 v[58:61], v[166:169], v[236:239], v[58:61]
	v_mfma_f32_16x16x32_bf16 v[50:53], v[174:177], v[236:239], v[50:53]
	s_waitcnt vmcnt(11)
	v_cvt_pk_bf16_f32 v248, v26, v27
	v_cvt_pk_bf16_f32 v249, v28, v29
	ds_write_b64 v205, v[248:249]
	s_add_u32 s70, s68, 0x2000
	s_addc_u32 s71, s69, 0
	global_load_dwordx4 v[26:29], v189, s[70:71]
	s_waitcnt lgkmcnt(7)
	v_mfma_f32_16x16x32_bf16 v[42:45], v[166:169], v[244:247], v[42:45]
	v_mfma_f32_16x16x32_bf16 v[30:33], v[174:177], v[244:247], v[30:33]
	s_waitcnt vmcnt(11)
	v_cvt_pk_bf16_f32 v248, v34, v35
	v_cvt_pk_bf16_f32 v249, v36, v37
	ds_write_b64 v206, v[248:249]
	global_load_dwordx4 v[34:37], v189, s[68:69]
	s_setprio 0
.LBB0_730:
.Lswp_guE_tail:
	s_lshl_b64 s[40:41], s[38:39], 7
	s_add_u32 s40, s8, s40
	s_mov_b32 m0, s51
	s_waitcnt vmcnt(8)
	s_waitcnt lgkmcnt(0)
	s_barrier
	s_addc_u32 s41, s9, s41
	v_cndmask_b32_e64 v164, v178, v209, s[4:5]
	v_cndmask_b32_e64 v163, v180, v210, s[4:5]
	global_load_lds_dwordx4 v164, s[40:41]
	s_mov_b32 m0, s60
	v_cndmask_b32_e64 v162, v213, v208, s[4:5]
	global_load_lds_dwordx4 v163, s[40:41]
	v_cmp_ne_u32_e32 vcc, 0, v162
	s_mov_b64 s[96:97], vcc
	s_cbranch_vccnz .LBB0_732
	v_cndmask_b32_e64 v163, v182, v211, s[4:5]
	s_add_i32 m0, s51, 0x4000
	v_cndmask_b32_e64 v162, v184, v212, s[4:5]
	global_load_lds_dwordx4 v163, s[40:41]
	s_add_i32 m0, s51, 0x6000
	s_nop 0
	global_load_lds_dwordx4 v162, s[40:41]
.LBB0_732:
	s_cmp_lg_u64 s[2:3], 0
	s_cbranch_scc1 .Lswp_guO_half
	ds_read_b64_tr_b16 v[162:163], v190 offset:32768
	ds_read_b64_tr_b16 v[164:165], v191 offset:32768
	ds_read_b64_tr_b16 v[166:167], v190 offset:40960
	ds_read_b64_tr_b16 v[168:169], v191 offset:40960
	ds_read_b64_tr_b16 v[170:171], v192 offset:32768
	ds_read_b64_tr_b16 v[172:173], v193 offset:32768
	ds_read_b64_tr_b16 v[174:175], v192 offset:40960
	ds_read_b64_tr_b16 v[176:177], v193 offset:40960
	ds_read_b128 v[214:217], v207 offset:32768
	ds_read_b128 v[224:227], v207 offset:34816
	ds_read_b128 v[232:235], v207 offset:36864
	ds_read_b128 v[240:243], v207 offset:38912
	ds_read_b128 v[218:221], v207 offset:33792
	ds_read_b128 v[228:231], v207 offset:35840
	ds_read_b128 v[236:239], v207 offset:37888
	ds_read_b128 v[244:247], v207 offset:39936
	s_lshl_b64 s[2:3], s[38:39], 18
	s_add_u32 s4, s2, 0x40000
	s_addc_u32 s5, s3, 0
	s_add_u32 s2, s67, s4
	s_addc_u32 s3, s66, s5
	s_add_u32 s4, s35, s4
	s_addc_u32 s5, s34, s5
	s_setprio 1
	s_waitcnt lgkmcnt(7)
	v_mfma_f32_16x16x32_bf16 v[158:161], v[162:165], v[214:217], v[158:161]
	v_mfma_f32_16x16x32_bf16 v[154:157], v[170:173], v[214:217], v[154:157]
	ds_read_b128 v[214:217], v207 offset:49152
	s_waitcnt lgkmcnt(7)
	v_mfma_f32_16x16x32_bf16 v[146:149], v[162:165], v[224:227], v[146:149]
	v_mfma_f32_16x16x32_bf16 v[138:141], v[170:173], v[224:227], v[138:141]
	ds_read_b128 v[224:227], v207 offset:51200
	s_waitcnt lgkmcnt(7)
	v_mfma_f32_16x16x32_bf16 v[130:133], v[162:165], v[232:235], v[130:133]
	v_mfma_f32_16x16x32_bf16 v[122:125], v[170:173], v[232:235], v[122:125]
	ds_read_b128 v[232:235], v207 offset:53248
	s_waitcnt lgkmcnt(7)
	v_mfma_f32_16x16x32_bf16 v[114:117], v[162:165], v[240:243], v[114:117]
	v_mfma_f32_16x16x32_bf16 v[106:109], v[170:173], v[240:243], v[106:109]
	ds_read_b128 v[240:243], v207 offset:55296
	s_waitcnt lgkmcnt(7)
	v_mfma_f32_16x16x32_bf16 v[158:161], v[166:169], v[218:221], v[158:161]
	v_mfma_f32_16x16x32_bf16 v[154:157], v[174:177], v[218:221], v[154:157]
	ds_read_b128 v[218:221], v207 offset:50176
	s_waitcnt lgkmcnt(7)
	v_mfma_f32_16x16x32_bf16 v[146:149], v[166:169], v[228:231], v[146:149]
	v_mfma_f32_16x16x32_bf16 v[138:141], v[174:177], v[228:231], v[138:141]
	ds_read_b128 v[228:231], v207 offset:52224
	s_waitcnt lgkmcnt(7)
	v_mfma_f32_16x16x32_bf16 v[130:133], v[166:169], v[236:239], v[130:133]
	v_mfma_f32_16x16x32_bf16 v[122:125], v[174:177], v[236:239], v[122:125]
	ds_read_b128 v[236:239], v207 offset:54272
	s_waitcnt lgkmcnt(7)
	v_mfma_f32_16x16x32_bf16 v[114:117], v[166:169], v[244:247], v[114:117]
	v_mfma_f32_16x16x32_bf16 v[106:109], v[174:177], v[244:247], v[106:109]
	ds_read_b128 v[244:247], v207 offset:56320
	s_waitcnt lgkmcnt(7)
	v_mfma_f32_16x16x32_bf16 v[94:97], v[162:165], v[214:217], v[94:97]
	v_mfma_f32_16x16x32_bf16 v[86:89], v[170:173], v[214:217], v[86:89]
	ds_read_b128 v[214:217], v207 offset:32768
	s_waitcnt lgkmcnt(7)
	v_mfma_f32_16x16x32_bf16 v[78:81], v[162:165], v[224:227], v[78:81]
	v_mfma_f32_16x16x32_bf16 v[70:73], v[170:173], v[224:227], v[70:73]
	ds_read_b128 v[224:227], v207 offset:34816
	s_waitcnt lgkmcnt(7)
	v_mfma_f32_16x16x32_bf16 v[62:65], v[162:165], v[232:235], v[62:65]
	v_mfma_f32_16x16x32_bf16 v[54:57], v[170:173], v[232:235], v[54:57]
	ds_read_b128 v[232:235], v207 offset:36864
	s_waitcnt lgkmcnt(7)
	v_mfma_f32_16x16x32_bf16 v[46:49], v[162:165], v[240:243], v[46:49]
	v_mfma_f32_16x16x32_bf16 v[38:41], v[170:173], v[240:243], v[38:41]
	ds_read_b128 v[240:243], v207 offset:38912
	ds_read_b64_tr_b16 v[162:163], v190 offset:49152
	ds_read_b64_tr_b16 v[164:165], v191 offset:49152
	ds_read_b64_tr_b16 v[170:171], v192 offset:49152
	ds_read_b64_tr_b16 v[172:173], v193 offset:49152
	s_waitcnt lgkmcnt(11)
	v_mfma_f32_16x16x32_bf16 v[94:97], v[166:169], v[218:221], v[94:97]
	v_mfma_f32_16x16x32_bf16 v[86:89], v[174:177], v[218:221], v[86:89]
	ds_read_b128 v[218:221], v207 offset:33792
	s_waitcnt lgkmcnt(11)
	v_mfma_f32_16x16x32_bf16 v[78:81], v[166:169], v[228:231], v[78:81]
	v_mfma_f32_16x16x32_bf16 v[70:73], v[174:177], v[228:231], v[70:73]
	ds_read_b128 v[228:231], v207 offset:35840
	s_waitcnt lgkmcnt(11)
	v_mfma_f32_16x16x32_bf16 v[62:65], v[166:169], v[236:239], v[62:65]
	v_mfma_f32_16x16x32_bf16 v[54:57], v[174:177], v[236:239], v[54:57]
	ds_read_b128 v[236:239], v207 offset:37888
	s_waitcnt lgkmcnt(11)
	v_mfma_f32_16x16x32_bf16 v[46:49], v[166:169], v[244:247], v[46:49]
	v_mfma_f32_16x16x32_bf16 v[38:41], v[174:177], v[244:247], v[38:41]
	ds_read_b128 v[244:247], v207 offset:39936
	ds_read_b64_tr_b16 v[166:167], v190 offset:57344
	ds_read_b64_tr_b16 v[168:169], v191 offset:57344
	ds_read_b64_tr_b16 v[174:175], v192 offset:57344
	ds_read_b64_tr_b16 v[176:177], v193 offset:57344
	s_waitcnt lgkmcnt(8)
	v_mfma_f32_16x16x32_bf16 v[150:153], v[162:165], v[214:217], v[150:153]
	v_mfma_f32_16x16x32_bf16 v[142:145], v[170:173], v[214:217], v[142:145]
	ds_read_b128 v[214:217], v207 offset:49152
	v_mfma_f32_16x16x32_bf16 v[134:137], v[162:165], v[224:227], v[134:137]
	v_mfma_f32_16x16x32_bf16 v[126:129], v[170:173], v[224:227], v[126:129]
	ds_read_b128 v[224:227], v207 offset:51200
	v_mfma_f32_16x16x32_bf16 v[118:121], v[162:165], v[232:235], v[118:121]
	v_mfma_f32_16x16x32_bf16 v[110:113], v[170:173], v[232:235], v[110:113]
	ds_read_b128 v[232:235], v207 offset:53248
	v_mfma_f32_16x16x32_bf16 v[102:105], v[162:165], v[240:243], v[102:105]
	v_mfma_f32_16x16x32_bf16 v[98:101], v[170:173], v[240:243], v[98:101]
	ds_read_b128 v[240:243], v207 offset:55296
	s_waitcnt lgkmcnt(4)
	v_mfma_f32_16x16x32_bf16 v[150:153], v[166:169], v[218:221], v[150:153]
	v_mfma_f32_16x16x32_bf16 v[142:145], v[174:177], v[218:221], v[142:145]
	ds_read_b128 v[218:221], v207 offset:50176
	v_mfma_f32_16x16x32_bf16 v[134:137], v[166:169], v[228:231], v[134:137]
	v_mfma_f32_16x16x32_bf16 v[126:129], v[174:177], v[228:231], v[126:129]
	ds_read_b128 v[228:231], v207 offset:52224
	v_mfma_f32_16x16x32_bf16 v[118:121], v[166:169], v[236:239], v[118:121]
	v_mfma_f32_16x16x32_bf16 v[110:113], v[174:177], v[236:239], v[110:113]
	ds_read_b128 v[236:239], v207 offset:54272
	v_mfma_f32_16x16x32_bf16 v[102:105], v[166:169], v[244:247], v[102:105]
	v_mfma_f32_16x16x32_bf16 v[98:101], v[174:177], v[244:247], v[98:101]
	ds_read_b128 v[244:247], v207 offset:56320
	s_waitcnt lgkmcnt(7)
	v_mfma_f32_16x16x32_bf16 v[90:93], v[162:165], v[214:217], v[90:93]
	v_mfma_f32_16x16x32_bf16 v[82:85], v[170:173], v[214:217], v[82:85]
	s_waitcnt vmcnt(9)
	v_cvt_pk_bf16_f32 v248, v2, v3
	v_cvt_pk_bf16_f32 v249, v4, v5
	ds_write_b64 v197, v[248:249] offset:16384
	global_load_dwordx4 v[2:5], v189, s[2:3]
	s_waitcnt lgkmcnt(7)
	v_mfma_f32_16x16x32_bf16 v[74:77], v[162:165], v[224:227], v[74:77]
	v_mfma_f32_16x16x32_bf16 v[66:69], v[170:173], v[224:227], v[66:69]
	s_waitcnt vmcnt(9)
	v_cvt_pk_bf16_f32 v248, v6, v7
	v_cvt_pk_bf16_f32 v249, v8, v9
	ds_write_b64 v196, v[248:249] offset:16384
	global_load_dwordx4 v[6:9], v189, s[4:5]
	s_waitcnt lgkmcnt(7)
	v_mfma_f32_16x16x32_bf16 v[58:61], v[162:165], v[232:235], v[58:61]
	v_mfma_f32_16x16x32_bf16 v[50:53], v[170:173], v[232:235], v[50:53]
	s_waitcnt vmcnt(9)
	v_cvt_pk_bf16_f32 v248, v10, v11
	v_cvt_pk_bf16_f32 v249, v12, v13
	ds_write_b64 v197, v[248:249]
	s_add_u32 s98, s2, 0x2000
	s_addc_u32 s99, s3, 0
	global_load_dwordx4 v[10:13], v189, s[98:99]
	s_waitcnt lgkmcnt(7)
	v_mfma_f32_16x16x32_bf16 v[42:45], v[162:165], v[240:243], v[42:45]
	v_mfma_f32_16x16x32_bf16 v[30:33], v[170:173], v[240:243], v[30:33]
	s_waitcnt vmcnt(9)
	v_cvt_pk_bf16_f32 v248, v14, v15
	v_cvt_pk_bf16_f32 v249, v16, v17
	ds_write_b64 v195, v[248:249] offset:16384
	s_add_u32 s100, s4, 0x2000
	s_addc_u32 s101, s5, 0
	global_load_dwordx4 v[14:17], v189, s[100:101]
	s_waitcnt lgkmcnt(7)
	v_mfma_f32_16x16x32_bf16 v[90:93], v[166:169], v[218:221], v[90:93]
	v_mfma_f32_16x16x32_bf16 v[82:85], v[174:177], v[218:221], v[82:85]
	s_waitcnt vmcnt(9)
	v_cvt_pk_bf16_f32 v248, v18, v19
	v_cvt_pk_bf16_f32 v249, v20, v21
	ds_write_b64 v196, v[248:249]
	s_add_u32 s98, s2, 0x4000
	s_addc_u32 s99, s3, 0
	global_load_dwordx4 v[18:21], v189, s[98:99]
	s_waitcnt lgkmcnt(7)
	v_mfma_f32_16x16x32_bf16 v[74:77], v[166:169], v[228:231], v[74:77]
	v_mfma_f32_16x16x32_bf16 v[66:69], v[174:177], v[228:231], v[66:69]
	s_waitcnt vmcnt(9)
	v_cvt_pk_bf16_f32 v248, v22, v23
	v_cvt_pk_bf16_f32 v249, v24, v25
	ds_write_b64 v194, v[248:249] offset:16384
	s_add_u32 s100, s4, 0x4000
	s_addc_u32 s101, s5, 0
	global_load_dwordx4 v[22:25], v189, s[100:101]
	s_waitcnt lgkmcnt(7)
	v_mfma_f32_16x16x32_bf16 v[58:61], v[166:169], v[236:239], v[58:61]
	v_mfma_f32_16x16x32_bf16 v[50:53], v[174:177], v[236:239], v[50:53]
	s_waitcnt vmcnt(9)
	v_cvt_pk_bf16_f32 v248, v26, v27
	v_cvt_pk_bf16_f32 v249, v28, v29
	ds_write_b64 v195, v[248:249]
	s_add_u32 s98, s2, 0x6000
	s_addc_u32 s99, s3, 0
	global_load_dwordx4 v[26:29], v189, s[98:99]
	s_waitcnt lgkmcnt(7)
	v_mfma_f32_16x16x32_bf16 v[42:45], v[166:169], v[244:247], v[42:45]
	v_mfma_f32_16x16x32_bf16 v[30:33], v[174:177], v[244:247], v[30:33]
	s_waitcnt vmcnt(9)
	v_cvt_pk_bf16_f32 v248, v34, v35
	v_cvt_pk_bf16_f32 v249, v36, v37
	ds_write_b64 v194, v[248:249]
	s_add_u32 s100, s4, 0x6000
	s_addc_u32 s101, s5, 0
	global_load_dwordx4 v[34:37], v189, s[100:101]
	s_setprio 0
.LBB0_736:
.Lswp_guO_tail:
	s_waitcnt vmcnt(8)
	s_waitcnt lgkmcnt(0)
	s_barrier
	s_cmp_gt_u32 s17, 29
	s_cbranch_scc1 .LBB0_738
	s_mov_b32 s34, s17
	s_branch .LBB0_724

.Lswqd_guE:
	v_cvt_pk_bf16_f32 v2, v2, v3
	v_cvt_pk_bf16_f32 v3, v4, v5
	ds_write_b64 v199, v[2:3]
	v_cvt_pk_bf16_f32 v2, v6, v7
	v_cvt_pk_bf16_f32 v3, v8, v9
	ds_write_b64 v200, v[2:3]
	v_cvt_pk_bf16_f32 v2, v10, v11
	v_cvt_pk_bf16_f32 v3, v12, v13
	ds_write_b64 v201, v[2:3]
	v_cvt_pk_bf16_f32 v2, v14, v15
	v_cvt_pk_bf16_f32 v3, v16, v17
	ds_write_b64 v202, v[2:3]
	v_cvt_pk_bf16_f32 v2, v18, v19
	v_cvt_pk_bf16_f32 v3, v20, v21
	ds_write_b64 v203, v[2:3]
	v_cvt_pk_bf16_f32 v2, v22, v23
	v_cvt_pk_bf16_f32 v3, v24, v25
	ds_write_b64 v204, v[2:3]
	v_cvt_pk_bf16_f32 v2, v26, v27
	v_cvt_pk_bf16_f32 v3, v28, v29
	ds_write_b64 v205, v[2:3]
	v_cvt_pk_bf16_f32 v2, v34, v35
	v_cvt_pk_bf16_f32 v3, v36, v37
	ds_write_b64 v206, v[2:3]
	s_ashr_i32 s39, s38, 31
	s_lshl_b64 s[40:41], s[38:39], 18
	s_add_u32 s68, s67, s40
	s_addc_u32 s69, s66, s41
	s_add_u32 s40, s35, s40
	s_addc_u32 s41, s34, s41
	s_add_u32 s70, s68, 0x2000
	s_addc_u32 s71, s69, 0
	global_load_dwordx4 v[34:37], v189, s[68:69]
	s_add_u32 s72, s40, 0x2000
	global_load_dwordx4 v[22:25], v189, s[40:41]
	s_addc_u32 s73, s41, 0
	global_load_dwordx4 v[26:29], v189, s[70:71]
	s_add_u32 s70, s68, 0x4000
	s_addc_u32 s71, s69, 0
	global_load_dwordx4 v[14:17], v189, s[72:73]
	s_add_u32 s72, s40, 0x4000
	s_addc_u32 s73, s41, 0
	s_add_u32 s68, s68, 0x6000
	global_load_dwordx4 v[18:21], v189, s[70:71]
	s_addc_u32 s69, s69, 0
	global_load_dwordx4 v[6:9], v189, s[72:73]
	s_add_u32 s40, s40, 0x6000
	s_addc_u32 s41, s41, 0
	global_load_dwordx4 v[10:13], v189, s[68:69]
	global_load_dwordx4 v[2:5], v189, s[40:41]
	s_branch .Lswp_guE_tail

.Lswqd_guO:
	v_cvt_pk_bf16_f32 v34, v34, v35
	v_cvt_pk_bf16_f32 v35, v36, v37
	ds_write_b64 v194, v[34:35]
	v_cvt_pk_bf16_f32 v22, v22, v23
	v_cvt_pk_bf16_f32 v23, v24, v25
	ds_write_b64 v194, v[22:23] offset:16384
	v_cvt_pk_bf16_f32 v22, v26, v27
	v_cvt_pk_bf16_f32 v23, v28, v29
	ds_write_b64 v195, v[22:23]
	v_cvt_pk_bf16_f32 v14, v14, v15
	v_cvt_pk_bf16_f32 v15, v16, v17
	ds_write_b64 v195, v[14:15] offset:16384
	v_cvt_pk_bf16_f32 v14, v18, v19
	v_cvt_pk_bf16_f32 v15, v20, v21
	ds_write_b64 v196, v[14:15]
	v_cvt_pk_bf16_f32 v6, v6, v7
	v_cvt_pk_bf16_f32 v7, v8, v9
	ds_write_b64 v196, v[6:7] offset:16384
	v_cvt_pk_bf16_f32 v6, v10, v11
	v_cvt_pk_bf16_f32 v7, v12, v13
	ds_write_b64 v197, v[6:7]
	v_cvt_pk_bf16_f32 v2, v2, v3
	v_cvt_pk_bf16_f32 v3, v4, v5
	ds_write_b64 v197, v[2:3] offset:16384
	s_add_u32 s4, s35, s4
	s_addc_u32 s5, s34, s5
	s_add_u32 s34, s2, 0x2000
	s_addc_u32 s35, s3, 0
	global_load_dwordx4 v[2:5], v189, s[2:3]
	s_add_u32 s38, s4, 0x2000
	global_load_dwordx4 v[6:9], v189, s[4:5]
	s_addc_u32 s39, s5, 0
	global_load_dwordx4 v[10:13], v189, s[34:35]
	s_add_u32 s34, s2, 0x4000
	s_addc_u32 s35, s3, 0
	global_load_dwordx4 v[14:17], v189, s[38:39]
	s_add_u32 s38, s4, 0x4000
	s_addc_u32 s39, s5, 0
	global_load_dwordx4 v[18:21], v189, s[34:35]
	s_add_u32 s2, s2, 0x6000
	global_load_dwordx4 v[22:25], v189, s[38:39]
	s_addc_u32 s3, s3, 0
	s_add_u32 s4, s4, 0x6000
	global_load_dwordx4 v[26:29], v189, s[2:3]
	s_addc_u32 s5, s5, 0
	global_load_dwordx4 v[34:37], v189, s[4:5]
	s_branch .Lswp_guO_tail

.LBB0_858:
	s_cmp_lg_u64 s[2:3], 0
	s_cbranch_scc1 .Lswp_dnE_half
	ds_read_b64_tr_b16 v[164:165], v190 offset:0
	ds_read_b64_tr_b16 v[166:167], v191 offset:0
	ds_read_b64_tr_b16 v[168:169], v190 offset:8192
	ds_read_b64_tr_b16 v[170:171], v191 offset:8192
	ds_read_b64_tr_b16 v[172:173], v192 offset:0
	ds_read_b64_tr_b16 v[174:175], v193 offset:0
	ds_read_b64_tr_b16 v[176:177], v192 offset:8192
	ds_read_b64_tr_b16 v[178:179], v193 offset:8192
	ds_read_b128 v[210:213], v207
	ds_read_b128 v[218:221], v207 offset:2048
	ds_read_b128 v[228:231], v207 offset:4096
	ds_read_b128 v[236:239], v207 offset:6144
	ds_read_b128 v[214:217], v207 offset:1024
	ds_read_b128 v[224:227], v207 offset:3072
	ds_read_b128 v[232:235], v207 offset:5120
	ds_read_b128 v[240:243], v207 offset:7168
	s_add_i32 s48, s48, 2
	s_cmp_eq_u32 s35, 12
	s_cselect_b32 s48, 0, s48
	s_cselect_b32 s77, s41, s23
	s_cselect_b32 s82, s40, s22
	s_cselect_b32 s35, s39, s47
	s_cselect_b32 s37, s38, s46
	s_cselect_b32 s43, s27, s45
	s_cselect_b32 s74, s26, s44
	s_cselect_b64 vcc, -1, 0
	s_ashr_i32 s49, s48, 31
	s_lshl_b64 s[50:51], s[48:49], 19
	s_add_u32 s72, s74, s50
	s_addc_u32 s73, s43, s51
	s_add_u32 s50, s37, s50
	s_addc_u32 s51, s35, s51
	s_setprio 1
	s_waitcnt lgkmcnt(7)
	v_mfma_f32_16x16x32_bf16 v[160:163], v[164:167], v[210:213], v[160:163]
	v_mfma_f32_16x16x32_bf16 v[156:159], v[172:175], v[210:213], v[156:159]
	ds_read_b128 v[210:213], v207 offset:16384
	s_waitcnt lgkmcnt(7)
	v_mfma_f32_16x16x32_bf16 v[152:155], v[164:167], v[218:221], v[152:155]
	v_mfma_f32_16x16x32_bf16 v[148:151], v[172:175], v[218:221], v[148:151]
	ds_read_b128 v[218:221], v207 offset:18432
	s_waitcnt lgkmcnt(7)
	v_mfma_f32_16x16x32_bf16 v[136:139], v[164:167], v[228:231], v[136:139]
	v_mfma_f32_16x16x32_bf16 v[132:135], v[172:175], v[228:231], v[132:135]
	ds_read_b128 v[228:231], v207 offset:20480
	s_waitcnt lgkmcnt(7)
	v_mfma_f32_16x16x32_bf16 v[120:123], v[164:167], v[236:239], v[120:123]
	v_mfma_f32_16x16x32_bf16 v[116:119], v[172:175], v[236:239], v[116:119]
	ds_read_b128 v[236:239], v207 offset:22528
	s_waitcnt lgkmcnt(7)
	v_mfma_f32_16x16x32_bf16 v[160:163], v[168:171], v[214:217], v[160:163]
	v_mfma_f32_16x16x32_bf16 v[156:159], v[176:179], v[214:217], v[156:159]
	ds_read_b128 v[214:217], v207 offset:17408
	s_waitcnt lgkmcnt(7)
	v_mfma_f32_16x16x32_bf16 v[152:155], v[168:171], v[224:227], v[152:155]
	v_mfma_f32_16x16x32_bf16 v[148:151], v[176:179], v[224:227], v[148:151]
	ds_read_b128 v[224:227], v207 offset:19456
	s_waitcnt lgkmcnt(7)
	v_mfma_f32_16x16x32_bf16 v[136:139], v[168:171], v[232:235], v[136:139]
	v_mfma_f32_16x16x32_bf16 v[132:135], v[176:179], v[232:235], v[132:135]
	ds_read_b128 v[232:235], v207 offset:21504
	s_waitcnt lgkmcnt(7)
	v_mfma_f32_16x16x32_bf16 v[120:123], v[168:171], v[240:243], v[120:123]
	v_mfma_f32_16x16x32_bf16 v[116:119], v[176:179], v[240:243], v[116:119]
	ds_read_b128 v[240:243], v207 offset:23552
	s_waitcnt lgkmcnt(7)
	v_mfma_f32_16x16x32_bf16 v[80:83], v[164:167], v[210:213], v[80:83]
	v_mfma_f32_16x16x32_bf16 v[68:71], v[172:175], v[210:213], v[68:71]
	ds_read_b128 v[210:213], v207
	s_waitcnt lgkmcnt(7)
	v_mfma_f32_16x16x32_bf16 v[48:51], v[164:167], v[218:221], v[48:51]
	v_mfma_f32_16x16x32_bf16 v[44:47], v[172:175], v[218:221], v[44:47]
	ds_read_b128 v[218:221], v207 offset:2048
	s_waitcnt lgkmcnt(7)
	v_mfma_f32_16x16x32_bf16 v[32:35], v[164:167], v[228:231], v[32:35]
	v_mfma_f32_16x16x32_bf16 v[28:31], v[172:175], v[228:231], v[28:31]
	ds_read_b128 v[228:231], v207 offset:4096
	s_waitcnt lgkmcnt(7)
	v_mfma_f32_16x16x32_bf16 v[16:19], v[164:167], v[236:239], v[16:19]
	v_mfma_f32_16x16x32_bf16 v[12:15], v[172:175], v[236:239], v[12:15]
	ds_read_b128 v[236:239], v207 offset:6144
	ds_read_b64_tr_b16 v[164:165], v190 offset:16384
	ds_read_b64_tr_b16 v[166:167], v191 offset:16384
	ds_read_b64_tr_b16 v[172:173], v192 offset:16384
	ds_read_b64_tr_b16 v[174:175], v193 offset:16384
	s_waitcnt lgkmcnt(11)
	v_mfma_f32_16x16x32_bf16 v[80:83], v[168:171], v[214:217], v[80:83]
	v_mfma_f32_16x16x32_bf16 v[68:71], v[176:179], v[214:217], v[68:71]
	ds_read_b128 v[214:217], v207 offset:1024
	s_waitcnt lgkmcnt(11)
	v_mfma_f32_16x16x32_bf16 v[48:51], v[168:171], v[224:227], v[48:51]
	v_mfma_f32_16x16x32_bf16 v[44:47], v[176:179], v[224:227], v[44:47]
	ds_read_b128 v[224:227], v207 offset:3072
	s_waitcnt lgkmcnt(11)
	v_mfma_f32_16x16x32_bf16 v[32:35], v[168:171], v[232:235], v[32:35]
	v_mfma_f32_16x16x32_bf16 v[28:31], v[176:179], v[232:235], v[28:31]
	ds_read_b128 v[232:235], v207 offset:5120
	s_waitcnt lgkmcnt(11)
	v_mfma_f32_16x16x32_bf16 v[16:19], v[168:171], v[240:243], v[16:19]
	v_mfma_f32_16x16x32_bf16 v[12:15], v[176:179], v[240:243], v[12:15]
	ds_read_b128 v[240:243], v207 offset:7168
	ds_read_b64_tr_b16 v[168:169], v190 offset:24576
	ds_read_b64_tr_b16 v[170:171], v191 offset:24576
	ds_read_b64_tr_b16 v[176:177], v192 offset:24576
	ds_read_b64_tr_b16 v[178:179], v193 offset:24576
	s_waitcnt lgkmcnt(8)
	v_mfma_f32_16x16x32_bf16 v[144:147], v[164:167], v[210:213], v[144:147]
	v_mfma_f32_16x16x32_bf16 v[140:143], v[172:175], v[210:213], v[140:143]
	ds_read_b128 v[210:213], v207 offset:16384
	v_mfma_f32_16x16x32_bf16 v[128:131], v[164:167], v[218:221], v[128:131]
	v_mfma_f32_16x16x32_bf16 v[124:127], v[172:175], v[218:221], v[124:127]
	ds_read_b128 v[218:221], v207 offset:18432
	v_mfma_f32_16x16x32_bf16 v[112:115], v[164:167], v[228:231], v[112:115]
	v_mfma_f32_16x16x32_bf16 v[108:111], v[172:175], v[228:231], v[108:111]
	ds_read_b128 v[228:231], v207 offset:20480
	v_mfma_f32_16x16x32_bf16 v[104:107], v[164:167], v[236:239], v[104:107]
	v_mfma_f32_16x16x32_bf16 v[100:103], v[172:175], v[236:239], v[100:103]
	ds_read_b128 v[236:239], v207 offset:22528
	s_waitcnt lgkmcnt(4)
	v_mfma_f32_16x16x32_bf16 v[144:147], v[168:171], v[214:217], v[144:147]
	v_mfma_f32_16x16x32_bf16 v[140:143], v[176:179], v[214:217], v[140:143]
	ds_read_b128 v[214:217], v207 offset:17408
	v_mfma_f32_16x16x32_bf16 v[128:131], v[168:171], v[224:227], v[128:131]
	v_mfma_f32_16x16x32_bf16 v[124:127], v[176:179], v[224:227], v[124:127]
	ds_read_b128 v[224:227], v207 offset:19456
	v_mfma_f32_16x16x32_bf16 v[112:115], v[168:171], v[232:235], v[112:115]
	v_mfma_f32_16x16x32_bf16 v[108:111], v[176:179], v[232:235], v[108:111]
	ds_read_b128 v[232:235], v207 offset:21504
	v_mfma_f32_16x16x32_bf16 v[104:107], v[168:171], v[240:243], v[104:107]
	v_mfma_f32_16x16x32_bf16 v[100:103], v[176:179], v[240:243], v[100:103]
	ds_read_b128 v[240:243], v207 offset:23552
	s_waitcnt lgkmcnt(7)
	v_mfma_f32_16x16x32_bf16 v[56:59], v[164:167], v[210:213], v[56:59]
	v_mfma_f32_16x16x32_bf16 v[52:55], v[172:175], v[210:213], v[52:55]
	s_waitcnt vmcnt(11)
	v_cvt_pk_bf16_f32 v244, v64, v65
	v_cvt_pk_bf16_f32 v245, v66, v67
	ds_write_b64 v199, v[244:245]
	s_add_u32 s78, s50, 0x8000
	s_addc_u32 s79, s51, 0
	global_load_dwordx4 v[64:67], v189, s[78:79]
	s_waitcnt lgkmcnt(7)
	v_mfma_f32_16x16x32_bf16 v[40:43], v[164:167], v[218:221], v[40:43]
	v_mfma_f32_16x16x32_bf16 v[36:39], v[172:175], v[218:221], v[36:39]
	s_waitcnt vmcnt(11)
	v_cvt_pk_bf16_f32 v244, v60, v61
	v_cvt_pk_bf16_f32 v245, v62, v63
	ds_write_b64 v200, v[244:245]
	s_add_u32 s80, s50, 0xc000
	s_addc_u32 s81, s51, 0
	global_load_dwordx4 v[60:63], v189, s[80:81]
	s_waitcnt lgkmcnt(7)
	v_mfma_f32_16x16x32_bf16 v[24:27], v[164:167], v[228:231], v[24:27]
	v_mfma_f32_16x16x32_bf16 v[20:23], v[172:175], v[228:231], v[20:23]
	s_waitcnt vmcnt(11)
	v_cvt_pk_bf16_f32 v244, v76, v77
	v_cvt_pk_bf16_f32 v245, v78, v79
	ds_write_b64 v201, v[244:245]
	s_add_u32 s78, s50, 0x4000
	s_addc_u32 s79, s51, 0
	global_load_dwordx4 v[76:79], v189, s[78:79]
	s_waitcnt lgkmcnt(7)
	v_mfma_f32_16x16x32_bf16 v[8:11], v[164:167], v[236:239], v[8:11]
	v_mfma_f32_16x16x32_bf16 v[2:5], v[172:175], v[236:239], v[4:7]
	s_waitcnt vmcnt(11)
	v_cvt_pk_bf16_f32 v244, v72, v73
	v_cvt_pk_bf16_f32 v245, v74, v75
	ds_write_b64 v202, v[244:245]
	s_add_u32 s80, s72, 0xc000
	s_addc_u32 s81, s73, 0
	global_load_dwordx4 v[72:75], v189, s[80:81]
	s_waitcnt lgkmcnt(7)
	v_mfma_f32_16x16x32_bf16 v[56:59], v[168:171], v[214:217], v[56:59]
	v_mfma_f32_16x16x32_bf16 v[52:55], v[176:179], v[214:217], v[52:55]
	s_waitcnt vmcnt(11)
	v_cvt_pk_bf16_f32 v244, v88, v89
	v_cvt_pk_bf16_f32 v245, v90, v91
	ds_write_b64 v203, v[244:245]
	global_load_dwordx4 v[88:91], v189, s[50:51]
	s_waitcnt lgkmcnt(7)
	v_mfma_f32_16x16x32_bf16 v[40:43], v[168:171], v[224:227], v[40:43]
	v_mfma_f32_16x16x32_bf16 v[36:39], v[176:179], v[224:227], v[36:39]
	s_waitcnt vmcnt(11)
	v_cvt_pk_bf16_f32 v244, v84, v85
	v_cvt_pk_bf16_f32 v245, v86, v87
	ds_write_b64 v204, v[244:245]
	s_add_u32 s80, s72, 0x8000
	s_addc_u32 s81, s73, 0
	global_load_dwordx4 v[84:87], v189, s[80:81]
	s_waitcnt lgkmcnt(7)
	v_mfma_f32_16x16x32_bf16 v[24:27], v[168:171], v[232:235], v[24:27]
	v_mfma_f32_16x16x32_bf16 v[20:23], v[176:179], v[232:235], v[20:23]
	s_waitcnt vmcnt(11)
	v_cvt_pk_bf16_f32 v244, v96, v97
	v_cvt_pk_bf16_f32 v245, v98, v99
	ds_write_b64 v205, v[244:245]
	global_load_dwordx4 v[96:99], v189, s[72:73]
	s_waitcnt lgkmcnt(7)
	v_mfma_f32_16x16x32_bf16 v[8:11], v[168:171], v[240:243], v[8:11]
	v_mfma_f32_16x16x32_bf16 v[4:7], v[176:179], v[240:243], v[2:5]
	s_waitcnt vmcnt(11)
	v_cvt_pk_bf16_f32 v244, v92, v93
	v_cvt_pk_bf16_f32 v245, v94, v95
	ds_write_b64 v206, v[244:245]
	s_add_u32 s80, s72, 0x4000
	s_addc_u32 s81, s73, 0
	global_load_dwordx4 v[92:95], v189, s[80:81]
	s_setprio 0
.LBB0_862:
.Lswp_dnE_tail:
	s_lshl_b64 s[50:51], s[48:49], 7
	s_add_u32 s50, s82, s50
	s_addc_u32 s51, s77, s51
	s_mov_b32 m0, s21
	s_waitcnt vmcnt(8)
	s_waitcnt lgkmcnt(0)
	s_barrier
	v_lshl_add_u64 v[2:3], s[50:51], 0, v[180:181]
	global_load_lds_dwordx4 v[2:3], off
	v_lshl_add_u64 v[2:3], s[50:51], 0, v[182:183]
	s_mov_b32 m0, s67
	v_cndmask_b32_e32 v1, v209, v208, vcc
	global_load_lds_dwordx4 v[2:3], off
	v_cmp_ne_u32_e32 vcc, 0, v1
	s_mov_b64 s[96:97], vcc
	s_cbranch_vccnz .LBB0_864
	v_lshl_add_u64 v[164:165], s[50:51], 0, v[184:185]
	s_add_i32 m0, s21, 0x4000
	v_lshl_add_u64 v[2:3], s[50:51], 0, v[186:187]
	global_load_lds_dwordx4 v[164:165], off
	s_add_i32 m0, s21, 0x6000
	s_nop 0
	global_load_lds_dwordx4 v[2:3], off
.LBB0_864:
	s_cmp_lg_u64 s[2:3], 0
	s_cbranch_scc1 .Lswp_dnO_half
	ds_read_b64_tr_b16 v[164:165], v190 offset:32768
	ds_read_b64_tr_b16 v[166:167], v191 offset:32768
	ds_read_b64_tr_b16 v[168:169], v190 offset:40960
	ds_read_b64_tr_b16 v[170:171], v191 offset:40960
	ds_read_b64_tr_b16 v[172:173], v192 offset:32768
	ds_read_b64_tr_b16 v[174:175], v193 offset:32768
	ds_read_b64_tr_b16 v[176:177], v192 offset:40960
	ds_read_b64_tr_b16 v[178:179], v193 offset:40960
	ds_read_b128 v[210:213], v207 offset:32768
	ds_read_b128 v[218:221], v207 offset:34816
	ds_read_b128 v[228:231], v207 offset:36864
	ds_read_b128 v[236:239], v207 offset:38912
	ds_read_b128 v[214:217], v207 offset:33792
	ds_read_b128 v[224:227], v207 offset:35840
	ds_read_b128 v[232:235], v207 offset:37888
	ds_read_b128 v[240:243], v207 offset:39936
	s_lshl_b64 s[2:3], s[48:49], 19
	s_add_u32 s48, s2, 0x80000
	s_addc_u32 s49, s3, 0
	s_add_u32 s2, s74, s48
	s_addc_u32 s3, s43, s49
	s_add_u32 s48, s37, s48
	s_addc_u32 s49, s35, s49
	s_setprio 1
	s_waitcnt lgkmcnt(7)
	v_mfma_f32_16x16x32_bf16 v[160:163], v[164:167], v[210:213], v[160:163]
	v_mfma_f32_16x16x32_bf16 v[156:159], v[172:175], v[210:213], v[156:159]
	ds_read_b128 v[210:213], v207 offset:49152
	s_waitcnt lgkmcnt(7)
	v_mfma_f32_16x16x32_bf16 v[152:155], v[164:167], v[218:221], v[152:155]
	v_mfma_f32_16x16x32_bf16 v[148:151], v[172:175], v[218:221], v[148:151]
	ds_read_b128 v[218:221], v207 offset:51200
	s_waitcnt lgkmcnt(7)
	v_mfma_f32_16x16x32_bf16 v[136:139], v[164:167], v[228:231], v[136:139]
	v_mfma_f32_16x16x32_bf16 v[132:135], v[172:175], v[228:231], v[132:135]
	ds_read_b128 v[228:231], v207 offset:53248
	s_waitcnt lgkmcnt(7)
	v_mfma_f32_16x16x32_bf16 v[120:123], v[164:167], v[236:239], v[120:123]
	v_mfma_f32_16x16x32_bf16 v[116:119], v[172:175], v[236:239], v[116:119]
	ds_read_b128 v[236:239], v207 offset:55296
	s_waitcnt lgkmcnt(7)
	v_mfma_f32_16x16x32_bf16 v[160:163], v[168:171], v[214:217], v[160:163]
	v_mfma_f32_16x16x32_bf16 v[156:159], v[176:179], v[214:217], v[156:159]
	ds_read_b128 v[214:217], v207 offset:50176
	s_waitcnt lgkmcnt(7)
	v_mfma_f32_16x16x32_bf16 v[152:155], v[168:171], v[224:227], v[152:155]
	v_mfma_f32_16x16x32_bf16 v[148:151], v[176:179], v[224:227], v[148:151]
	ds_read_b128 v[224:227], v207 offset:52224
	s_waitcnt lgkmcnt(7)
	v_mfma_f32_16x16x32_bf16 v[136:139], v[168:171], v[232:235], v[136:139]
	v_mfma_f32_16x16x32_bf16 v[132:135], v[176:179], v[232:235], v[132:135]
	ds_read_b128 v[232:235], v207 offset:54272
	s_waitcnt lgkmcnt(7)
	v_mfma_f32_16x16x32_bf16 v[120:123], v[168:171], v[240:243], v[120:123]
	v_mfma_f32_16x16x32_bf16 v[116:119], v[176:179], v[240:243], v[116:119]
	ds_read_b128 v[240:243], v207 offset:56320
	s_waitcnt lgkmcnt(7)
	v_mfma_f32_16x16x32_bf16 v[80:83], v[164:167], v[210:213], v[80:83]
	v_mfma_f32_16x16x32_bf16 v[68:71], v[172:175], v[210:213], v[68:71]
	ds_read_b128 v[210:213], v207 offset:32768
	s_waitcnt lgkmcnt(7)
	v_mfma_f32_16x16x32_bf16 v[48:51], v[164:167], v[218:221], v[48:51]
	v_mfma_f32_16x16x32_bf16 v[44:47], v[172:175], v[218:221], v[44:47]
	ds_read_b128 v[218:221], v207 offset:34816
	s_waitcnt lgkmcnt(7)
	v_mfma_f32_16x16x32_bf16 v[32:35], v[164:167], v[228:231], v[32:35]
	v_mfma_f32_16x16x32_bf16 v[28:31], v[172:175], v[228:231], v[28:31]
	ds_read_b128 v[228:231], v207 offset:36864
	s_waitcnt lgkmcnt(7)
	v_mfma_f32_16x16x32_bf16 v[16:19], v[164:167], v[236:239], v[16:19]
	v_mfma_f32_16x16x32_bf16 v[12:15], v[172:175], v[236:239], v[12:15]
	ds_read_b128 v[236:239], v207 offset:38912
	ds_read_b64_tr_b16 v[164:165], v190 offset:49152
	ds_read_b64_tr_b16 v[166:167], v191 offset:49152
	ds_read_b64_tr_b16 v[172:173], v192 offset:49152
	ds_read_b64_tr_b16 v[174:175], v193 offset:49152
	s_waitcnt lgkmcnt(11)
	v_mfma_f32_16x16x32_bf16 v[80:83], v[168:171], v[214:217], v[80:83]
	v_mfma_f32_16x16x32_bf16 v[68:71], v[176:179], v[214:217], v[68:71]
	ds_read_b128 v[214:217], v207 offset:33792
	s_waitcnt lgkmcnt(11)
	v_mfma_f32_16x16x32_bf16 v[48:51], v[168:171], v[224:227], v[48:51]
	v_mfma_f32_16x16x32_bf16 v[44:47], v[176:179], v[224:227], v[44:47]
	ds_read_b128 v[224:227], v207 offset:35840
	s_waitcnt lgkmcnt(11)
	v_mfma_f32_16x16x32_bf16 v[32:35], v[168:171], v[232:235], v[32:35]
	v_mfma_f32_16x16x32_bf16 v[28:31], v[176:179], v[232:235], v[28:31]
	ds_read_b128 v[232:235], v207 offset:37888
	s_waitcnt lgkmcnt(11)
	v_mfma_f32_16x16x32_bf16 v[16:19], v[168:171], v[240:243], v[16:19]
	v_mfma_f32_16x16x32_bf16 v[12:15], v[176:179], v[240:243], v[12:15]
	ds_read_b128 v[240:243], v207 offset:39936
	ds_read_b64_tr_b16 v[168:169], v190 offset:57344
	ds_read_b64_tr_b16 v[170:171], v191 offset:57344
	ds_read_b64_tr_b16 v[176:177], v192 offset:57344
	ds_read_b64_tr_b16 v[178:179], v193 offset:57344
	s_waitcnt lgkmcnt(8)
	v_mfma_f32_16x16x32_bf16 v[144:147], v[164:167], v[210:213], v[144:147]
	v_mfma_f32_16x16x32_bf16 v[140:143], v[172:175], v[210:213], v[140:143]
	ds_read_b128 v[210:213], v207 offset:49152
	v_mfma_f32_16x16x32_bf16 v[128:131], v[164:167], v[218:221], v[128:131]
	v_mfma_f32_16x16x32_bf16 v[124:127], v[172:175], v[218:221], v[124:127]
	ds_read_b128 v[218:221], v207 offset:51200
	v_mfma_f32_16x16x32_bf16 v[112:115], v[164:167], v[228:231], v[112:115]
	v_mfma_f32_16x16x32_bf16 v[108:111], v[172:175], v[228:231], v[108:111]
	ds_read_b128 v[228:231], v207 offset:53248
	v_mfma_f32_16x16x32_bf16 v[104:107], v[164:167], v[236:239], v[104:107]
	v_mfma_f32_16x16x32_bf16 v[100:103], v[172:175], v[236:239], v[100:103]
	ds_read_b128 v[236:239], v207 offset:55296
	s_waitcnt lgkmcnt(4)
	v_mfma_f32_16x16x32_bf16 v[144:147], v[168:171], v[214:217], v[144:147]
	v_mfma_f32_16x16x32_bf16 v[140:143], v[176:179], v[214:217], v[140:143]
	ds_read_b128 v[214:217], v207 offset:50176
	v_mfma_f32_16x16x32_bf16 v[128:131], v[168:171], v[224:227], v[128:131]
	v_mfma_f32_16x16x32_bf16 v[124:127], v[176:179], v[224:227], v[124:127]
	ds_read_b128 v[224:227], v207 offset:52224
	v_mfma_f32_16x16x32_bf16 v[112:115], v[168:171], v[232:235], v[112:115]
	v_mfma_f32_16x16x32_bf16 v[108:111], v[176:179], v[232:235], v[108:111]
	ds_read_b128 v[232:235], v207 offset:54272
	v_mfma_f32_16x16x32_bf16 v[104:107], v[168:171], v[240:243], v[104:107]
	v_mfma_f32_16x16x32_bf16 v[100:103], v[176:179], v[240:243], v[100:103]
	ds_read_b128 v[240:243], v207 offset:56320
	s_waitcnt lgkmcnt(7)
	v_mfma_f32_16x16x32_bf16 v[56:59], v[164:167], v[210:213], v[56:59]
	v_mfma_f32_16x16x32_bf16 v[52:55], v[172:175], v[210:213], v[52:55]
	s_waitcnt vmcnt(9)
	v_cvt_pk_bf16_f32 v244, v64, v65
	v_cvt_pk_bf16_f32 v245, v66, v67
	ds_write_b64 v196, v[244:245] offset:16384
	global_load_dwordx4 v[64:67], v189, s[2:3]
	s_waitcnt lgkmcnt(7)
	v_mfma_f32_16x16x32_bf16 v[40:43], v[164:167], v[218:221], v[40:43]
	v_mfma_f32_16x16x32_bf16 v[36:39], v[172:175], v[218:221], v[36:39]
	s_waitcnt vmcnt(9)
	v_cvt_pk_bf16_f32 v244, v60, v61
	v_cvt_pk_bf16_f32 v245, v62, v63
	ds_write_b64 v197, v[244:245] offset:16384
	global_load_dwordx4 v[60:63], v189, s[48:49]
	s_waitcnt lgkmcnt(7)
	v_mfma_f32_16x16x32_bf16 v[24:27], v[164:167], v[228:231], v[24:27]
	v_mfma_f32_16x16x32_bf16 v[20:23], v[172:175], v[228:231], v[20:23]
	s_waitcnt vmcnt(9)
	v_cvt_pk_bf16_f32 v244, v76, v77
	v_cvt_pk_bf16_f32 v245, v78, v79
	ds_write_b64 v195, v[244:245] offset:16384
	s_add_u32 s98, s2, 0x4000
	s_addc_u32 s99, s3, 0
	global_load_dwordx4 v[76:79], v189, s[98:99]
	s_waitcnt lgkmcnt(7)
	v_mfma_f32_16x16x32_bf16 v[8:11], v[164:167], v[236:239], v[8:11]
	v_mfma_f32_16x16x32_bf16 v[2:5], v[172:175], v[236:239], v[4:7]
	s_waitcnt vmcnt(9)
	v_cvt_pk_bf16_f32 v244, v72, v73
	v_cvt_pk_bf16_f32 v245, v74, v75
	ds_write_b64 v197, v[244:245]
	s_add_u32 s100, s48, 0x4000
	s_addc_u32 s101, s49, 0
	global_load_dwordx4 v[72:75], v189, s[100:101]
	s_waitcnt lgkmcnt(7)
	v_mfma_f32_16x16x32_bf16 v[56:59], v[168:171], v[214:217], v[56:59]
	v_mfma_f32_16x16x32_bf16 v[52:55], v[176:179], v[214:217], v[52:55]
	s_waitcnt vmcnt(9)
	v_cvt_pk_bf16_f32 v244, v88, v89
	v_cvt_pk_bf16_f32 v245, v90, v91
	ds_write_b64 v194, v[244:245] offset:16384
	s_add_u32 s98, s2, 0x8000
	s_addc_u32 s99, s3, 0
	global_load_dwordx4 v[88:91], v189, s[98:99]
	s_waitcnt lgkmcnt(7)
	v_mfma_f32_16x16x32_bf16 v[40:43], v[168:171], v[224:227], v[40:43]
	v_mfma_f32_16x16x32_bf16 v[36:39], v[176:179], v[224:227], v[36:39]
	s_waitcnt vmcnt(9)
	v_cvt_pk_bf16_f32 v244, v84, v85
	v_cvt_pk_bf16_f32 v245, v86, v87
	ds_write_b64 v196, v[244:245]
	s_add_u32 s100, s48, 0x8000
	s_addc_u32 s101, s49, 0
	global_load_dwordx4 v[84:87], v189, s[100:101]
	s_waitcnt lgkmcnt(7)
	v_mfma_f32_16x16x32_bf16 v[24:27], v[168:171], v[232:235], v[24:27]
	v_mfma_f32_16x16x32_bf16 v[20:23], v[176:179], v[232:235], v[20:23]
	s_waitcnt vmcnt(9)
	v_cvt_pk_bf16_f32 v244, v96, v97
	v_cvt_pk_bf16_f32 v245, v98, v99
	ds_write_b64 v194, v[244:245]
	s_add_u32 s98, s2, 0xc000
	s_addc_u32 s99, s3, 0
	global_load_dwordx4 v[96:99], v189, s[98:99]
	s_waitcnt lgkmcnt(7)
	v_mfma_f32_16x16x32_bf16 v[8:11], v[168:171], v[240:243], v[8:11]
	v_mfma_f32_16x16x32_bf16 v[4:7], v[176:179], v[240:243], v[2:5]
	s_waitcnt vmcnt(9)
	v_cvt_pk_bf16_f32 v244, v92, v93
	v_cvt_pk_bf16_f32 v245, v94, v95
	ds_write_b64 v195, v[244:245]
	s_add_u32 s100, s48, 0xc000
	s_addc_u32 s101, s49, 0
	global_load_dwordx4 v[92:95], v189, s[100:101]
	s_setprio 0
.LBB0_868:
.Lswp_dnO_tail:
	s_waitcnt vmcnt(8)
	s_waitcnt lgkmcnt(0)
	s_barrier
	s_cmp_gt_u32 s34, 13
	s_cbranch_scc1 .LBB0_870
	s_mov_b32 s35, s34
	s_branch .LBB0_856

.Lswqd_dnE:
	v_cvt_pk_bf16_f32 v2, v64, v65
	v_cvt_pk_bf16_f32 v3, v66, v67
	ds_write_b64 v199, v[2:3]
	v_cvt_pk_bf16_f32 v2, v60, v61
	v_cvt_pk_bf16_f32 v3, v62, v63
	ds_write_b64 v200, v[2:3]
	v_cvt_pk_bf16_f32 v2, v76, v77
	v_cvt_pk_bf16_f32 v3, v78, v79
	ds_write_b64 v201, v[2:3]
	v_cvt_pk_bf16_f32 v2, v72, v73
	v_cvt_pk_bf16_f32 v3, v74, v75
	ds_write_b64 v202, v[2:3]
	v_cvt_pk_bf16_f32 v2, v88, v89
	v_cvt_pk_bf16_f32 v3, v90, v91
	ds_write_b64 v203, v[2:3]
	v_cvt_pk_bf16_f32 v2, v84, v85
	v_cvt_pk_bf16_f32 v3, v86, v87
	ds_write_b64 v204, v[2:3]
	v_cvt_pk_bf16_f32 v2, v96, v97
	v_cvt_pk_bf16_f32 v3, v98, v99
	ds_write_b64 v205, v[2:3]
	v_cvt_pk_bf16_f32 v2, v92, v93
	v_cvt_pk_bf16_f32 v3, v94, v95
	ds_write_b64 v206, v[2:3]
	s_ashr_i32 s49, s48, 31
	s_lshl_b64 s[50:51], s[48:49], 19
	s_add_u32 s72, s74, s50
	s_addc_u32 s73, s43, s51
	s_add_u32 s50, s37, s50
	s_addc_u32 s51, s35, s51
	s_add_u32 s78, s72, 0x4000
	s_addc_u32 s79, s73, 0
	global_load_dwordx4 v[96:99], v189, s[72:73]
	s_add_u32 s80, s50, 0x4000
	global_load_dwordx4 v[88:91], v189, s[50:51]
	s_addc_u32 s81, s51, 0
	global_load_dwordx4 v[92:95], v189, s[78:79]
	s_add_u32 s78, s72, 0x8000
	s_addc_u32 s79, s73, 0
	global_load_dwordx4 v[76:79], v189, s[80:81]
	s_add_u32 s80, s50, 0x8000
	s_addc_u32 s81, s51, 0
	s_add_u32 s72, s72, 0xc000
	global_load_dwordx4 v[84:87], v189, s[78:79]
	s_addc_u32 s73, s73, 0
	global_load_dwordx4 v[64:67], v189, s[80:81]
	s_add_u32 s50, s50, 0xc000
	s_addc_u32 s51, s51, 0
	global_load_dwordx4 v[72:75], v189, s[72:73]
	global_load_dwordx4 v[60:63], v189, s[50:51]
	s_branch .Lswp_dnE_tail

.Lswqd_dnO:
	v_cvt_pk_bf16_f32 v2, v96, v97
	v_cvt_pk_bf16_f32 v3, v98, v99
	ds_write_b64 v194, v[2:3]
	v_cvt_pk_bf16_f32 v2, v88, v89
	v_cvt_pk_bf16_f32 v3, v90, v91
	ds_write_b64 v194, v[2:3] offset:16384
	v_cvt_pk_bf16_f32 v2, v92, v93
	v_cvt_pk_bf16_f32 v3, v94, v95
	ds_write_b64 v195, v[2:3]
	v_cvt_pk_bf16_f32 v2, v76, v77
	v_cvt_pk_bf16_f32 v3, v78, v79
	ds_write_b64 v195, v[2:3] offset:16384
	v_cvt_pk_bf16_f32 v2, v84, v85
	v_cvt_pk_bf16_f32 v3, v86, v87
	ds_write_b64 v196, v[2:3]
	v_cvt_pk_bf16_f32 v2, v64, v65
	v_cvt_pk_bf16_f32 v3, v66, v67
	ds_write_b64 v196, v[2:3] offset:16384
	v_cvt_pk_bf16_f32 v2, v72, v73
	v_cvt_pk_bf16_f32 v3, v74, v75
	ds_write_b64 v197, v[2:3]
	v_cvt_pk_bf16_f32 v2, v60, v61
	v_cvt_pk_bf16_f32 v3, v62, v63
	ds_write_b64 v197, v[2:3] offset:16384
	s_add_u32 s48, s2, 0x80000
	s_addc_u32 s49, s3, 0
	s_add_u32 s2, s74, s48
	s_addc_u32 s3, s43, s49
	s_add_u32 s48, s37, s48
	s_addc_u32 s49, s35, s49
	s_add_u32 s50, s2, 0x4000
	s_addc_u32 s51, s3, 0
	global_load_dwordx4 v[64:67], v189, s[2:3]
	s_add_u32 s72, s48, 0x4000
	global_load_dwordx4 v[60:63], v189, s[48:49]
	s_addc_u32 s73, s49, 0
	global_load_dwordx4 v[76:79], v189, s[50:51]
	s_add_u32 s50, s2, 0x8000
	s_addc_u32 s51, s3, 0
	global_load_dwordx4 v[72:75], v189, s[72:73]
	s_add_u32 s72, s48, 0x8000
	s_addc_u32 s73, s49, 0
	global_load_dwordx4 v[88:91], v189, s[50:51]
	s_add_u32 s2, s2, 0xc000
	global_load_dwordx4 v[84:87], v189, s[72:73]
	s_addc_u32 s3, s3, 0
	s_add_u32 s48, s48, 0xc000
	global_load_dwordx4 v[96:99], v189, s[2:3]
	s_addc_u32 s49, s49, 0
	global_load_dwordx4 v[92:95], v189, s[48:49]
	s_branch .Lswp_dnO_tail
